# baseline (speedup 1.0000x reference)
amdhsa.kernels:
  - .agpr_count:     0
    .args:
      - .actual_access:  read_only
        .address_space:  global
        .offset:         0
        .size:           8
        .value_kind:     global_buffer
      - .actual_access:  read_only
        .address_space:  global
        .offset:         8
        .size:           8
        .value_kind:     global_buffer
      - .actual_access:  read_only
        .address_space:  global
        .offset:         16
        .size:           8
        .value_kind:     global_buffer
      - .actual_access:  read_only
        .address_space:  global
        .offset:         24
        .size:           8
        .value_kind:     global_buffer
      - .actual_access:  read_only
        .address_space:  global
        .offset:         32
        .size:           8
        .value_kind:     global_buffer
      - .actual_access:  read_only
        .address_space:  global
        .offset:         40
        .size:           8
        .value_kind:     global_buffer
      - .actual_access:  read_only
        .address_space:  global
        .offset:         48
        .size:           8
        .value_kind:     global_buffer
      - .actual_access:  read_only
        .address_space:  global
        .offset:         56
        .size:           8
        .value_kind:     global_buffer
      - .actual_access:  read_only
        .address_space:  global
        .offset:         64
        .size:           8
        .value_kind:     global_buffer
      - .actual_access:  write_only
        .address_space:  global
        .offset:         72
        .size:           8
        .value_kind:     global_buffer
      - .actual_access:  write_only
        .address_space:  global
        .offset:         80
        .size:           8
        .value_kind:     global_buffer
      - .actual_access:  read_only
        .address_space:  global
        .offset:         88
        .size:           8
        .value_kind:     global_buffer
    .group_segment_fixed_size: 16640
    .kernarg_segment_align: 8
    .kernarg_segment_size: 96
    .language:       OpenCL C
    .language_version:
      - 2
      - 0
    .max_flat_workgroup_size: 256
    .name:           _Z11prep_kernelPKfS0_S0_S0_S0_S0_S0_S0_P14__hip_bfloat16S2_PDF16_Pf
    .private_segment_fixed_size: 0
    .sgpr_count:     18
    .sgpr_spill_count: 0
    .symbol:         _Z11prep_kernelPKfS0_S0_S0_S0_S0_S0_S0_P14__hip_bfloat16S2_PDF16_Pf.kd
    .uniform_work_group_size: 1
    .uses_dynamic_stack: false
    .vgpr_count:     29
    .vgpr_spill_count: 0
    .wavefront_size: 64
  - .agpr_count:     0
    .args:
      - .actual_access:  read_only
        .address_space:  global
        .offset:         0
        .size:           8
        .value_kind:     global_buffer
      - .actual_access:  read_only
        .address_space:  global
        .offset:         8
        .size:           8
        .value_kind:     global_buffer
      - .actual_access:  read_only
        .address_space:  global
        .offset:         16
        .size:           8
        .value_kind:     global_buffer
      - .actual_access:  read_only
        .address_space:  global
        .offset:         24
        .size:           8
        .value_kind:     global_buffer
      - .actual_access:  read_only
        .address_space:  global
        .offset:         32
        .size:           8
        .value_kind:     global_buffer
      - .actual_access:  read_only
        .address_space:  global
        .offset:         40
        .size:           8
        .value_kind:     global_buffer
      - .actual_access:  read_only
        .address_space:  global
        .offset:         48
        .size:           8
        .value_kind:     global_buffer
      - .actual_access:  write_only
        .address_space:  global
        .offset:         56
        .size:           8
        .value_kind:     global_buffer
    .group_segment_fixed_size: 0
    .kernarg_segment_align: 8
    .kernarg_segment_size: 64
    .language:       OpenCL C
    .language_version:
      - 2
      - 0
    .max_flat_workgroup_size: 512
    .name:           _Z9proj_gemmPKfS0_S0_PK14__hip_bfloat16S0_S0_S0_PS1_
    .private_segment_fixed_size: 0
    .sgpr_count:     46
    .sgpr_spill_count: 0
    .symbol:         _Z9proj_gemmPKfS0_S0_PK14__hip_bfloat16S0_S0_S0_PS1_.kd
    .uniform_work_group_size: 1
    .uses_dynamic_stack: false
    .vgpr_count:     243
    .vgpr_spill_count: 0
    .wavefront_size: 64
  - .agpr_count:     256
    .args:
      - .address_space:  global
        .offset:         0
        .size:           8
        .value_kind:     global_buffer
      - .address_space:  global
        .offset:         8
        .size:           8
        .value_kind:     global_buffer
      - .address_space:  global
        .offset:         16
        .size:           8
        .value_kind:     global_buffer
      - .actual_access:  write_only
        .address_space:  global
        .offset:         24
        .size:           8
        .value_kind:     global_buffer
      - .offset:         32
        .size:           4
        .value_kind:     hidden_block_count_x
      - .offset:         36
        .size:           4
        .value_kind:     hidden_block_count_y
      - .offset:         40
        .size:           4
        .value_kind:     hidden_block_count_z
      - .offset:         44
        .size:           2
        .value_kind:     hidden_group_size_x
      - .offset:         46
        .size:           2
        .value_kind:     hidden_group_size_y
      - .offset:         48
        .size:           2
        .value_kind:     hidden_group_size_z
      - .offset:         50
        .size:           2
        .value_kind:     hidden_remainder_x
      - .offset:         52
        .size:           2
        .value_kind:     hidden_remainder_y
      - .offset:         54
        .size:           2
        .value_kind:     hidden_remainder_z
      - .offset:         72
        .size:           8
        .value_kind:     hidden_global_offset_x
      - .offset:         80
        .size:           8
        .value_kind:     hidden_global_offset_y
      - .offset:         88
        .size:           8
        .value_kind:     hidden_global_offset_z
      - .offset:         96
        .size:           2
        .value_kind:     hidden_grid_dims
      - .offset:         152
        .size:           4
        .value_kind:     hidden_dynamic_lds_size
    .group_segment_fixed_size: 0
    .kernarg_segment_align: 8
    .kernarg_segment_size: 288
    .language:       OpenCL C
    .language_version:
      - 2
      - 0
    .max_flat_workgroup_size: 256
    .name:           _ZN2pw16attn_fwd_pwg4x64EPKtS1_S1_Pf
    .private_segment_fixed_size: 0
    .sgpr_count:     101
    .sgpr_spill_count: 0
    .symbol:         _ZN2pw16attn_fwd_pwg4x64EPKtS1_S1_Pf.kd
    .uniform_work_group_size: 1
    .uses_dynamic_stack: false
    .vgpr_count:     508
    .vgpr_spill_count: 0
    .wavefront_size: 64
  - .agpr_count:     0
    .args:
      - .actual_access:  read_only
        .address_space:  global
        .offset:         0
        .size:           8
        .value_kind:     global_buffer
      - .actual_access:  read_only
        .address_space:  global
        .offset:         8
        .size:           8
        .value_kind:     global_buffer
      - .actual_access:  read_only
        .address_space:  global
        .offset:         16
        .size:           8
        .value_kind:     global_buffer
      - .actual_access:  write_only
        .address_space:  global
        .offset:         24
        .size:           8
        .value_kind:     global_buffer
    .group_segment_fixed_size: 0
    .kernarg_segment_align: 8
    .kernarg_segment_size: 32
    .language:       OpenCL C
    .language_version:
      - 2
      - 0
    .max_flat_workgroup_size: 512
    .name:           _Z8out_projPKDF16_S0_PKfPf
    .private_segment_fixed_size: 0
    .sgpr_count:     24
    .sgpr_spill_count: 0
    .symbol:         _Z8out_projPKDF16_S0_PKfPf.kd
    .uniform_work_group_size: 1
    .uses_dynamic_stack: false
    .vgpr_count:     256
    .vgpr_spill_count: 0
    .wavefront_size: 64
